# speedup vs baseline: 1.0090x; 1.0040x over previous
.LBB4_49:
	s_mov_b64 vcc, s[0:1]
	s_lshl_b32 s35, s82, 8
	s_add_i32 s35, s35, s65
	s_lshl_b32 s28, s81, 7
	s_or_b32 s28, s28, s66
	s_ashr_i32 s37, s35, 8
	s_ashr_i32 s28, s28, 6
	s_mul_i32 s37, s37, 44
	s_add_i32 s37, s37, s28
	s_lshl_b32 s37, s37, 1
	v_or_b32_e32 v188, s35, v232
	s_or_b32 s42, s37, s73
	s_ashr_i32 s43, s42, 31
	v_lshlrev_b32_e32 v189, 6, v188
	s_lshl_b64 s[42:43], s[42:43], 14
	v_and_or_b32 v186, v189, s71, v233
	v_lshlrev_b32_e32 v189, 2, v188
	v_and_b32_e32 v187, 32, v189
	s_add_u32 s42, s2, s42
	s_addc_u32 s43, s3, s43
	v_bitop3_b32 v182, v186, s74, v187 bitop3:0xde
	s_or_b32 s37, s35, 16
	s_lshr_b32 s37, s37, 3
	s_and_b32 s37, s37, 10
	s_or_b32 s37, s37, s72
	s_lshl_b32 s37, s37, 10
	v_bitop3_b32 v183, v186, s37, v187 bitop3:0xde
	s_or_b32 s37, s35, 32
	s_lshr_b32 s37, s37, 3
	s_and_b32 s37, s37, 12
	s_or_b32 s37, s37, s72
	s_lshl_b32 s37, s37, 10
	v_bitop3_b32 v184, v186, s37, v187 bitop3:0xde
	s_or_b32 s35, s35, 48
	s_lshr_b32 s35, s35, 3
	s_and_b32 s35, s35, 14
	s_or_b32 s35, s35, s72
	s_lshl_b32 s35, s35, 10
	v_bitop3_b32 v185, v186, s35, v187 bitop3:0xde
	s_add_u32 s94, s42, 0x4000
	s_addc_u32 s95, s43, 0
	v_mul_f32_e32 v134, 0xbfb8aa3b, v114
	v_mul_f32_e32 v135, 0xbfb8aa3b, v115
	v_mul_f32_e32 v136, 0xbfb8aa3b, v116
	v_mul_f32_e32 v137, 0xbfb8aa3b, v117
	v_mul_f32_e32 v138, 0xbfb8aa3b, v106
	v_mul_f32_e32 v139, 0xbfb8aa3b, v107
	v_mul_f32_e32 v140, 0xbfb8aa3b, v108
	v_mul_f32_e32 v141, 0xbfb8aa3b, v109
	v_mul_f32_e32 v142, 0xbfb8aa3b, v98
	v_mul_f32_e32 v143, 0xbfb8aa3b, v99
	v_mul_f32_e32 v144, 0xbfb8aa3b, v100
	v_mul_f32_e32 v145, 0xbfb8aa3b, v101
	v_mul_f32_e32 v146, 0xbfb8aa3b, v86
	v_mul_f32_e32 v147, 0xbfb8aa3b, v87
	v_mul_f32_e32 v148, 0xbfb8aa3b, v88
	v_mul_f32_e32 v149, 0xbfb8aa3b, v89
	v_exp_f32_e32 v134, v134
	v_exp_f32_e32 v135, v135
	v_exp_f32_e32 v136, v136
	v_exp_f32_e32 v137, v137
	v_exp_f32_e32 v138, v138
	v_exp_f32_e32 v139, v139
	v_exp_f32_e32 v140, v140
	v_exp_f32_e32 v141, v141
	v_exp_f32_e32 v142, v142
	v_exp_f32_e32 v143, v143
	v_exp_f32_e32 v144, v144
	v_exp_f32_e32 v145, v145
	v_exp_f32_e32 v146, v146
	v_exp_f32_e32 v147, v147
	v_exp_f32_e32 v148, v148
	v_exp_f32_e32 v149, v149
	v_add_f32_e32 v134, 1.0, v134
	v_add_f32_e32 v135, 1.0, v135
	v_add_f32_e32 v136, 1.0, v136
	v_add_f32_e32 v137, 1.0, v137
	v_add_f32_e32 v138, 1.0, v138
	v_add_f32_e32 v139, 1.0, v139
	v_add_f32_e32 v140, 1.0, v140
	v_add_f32_e32 v141, 1.0, v141
	v_add_f32_e32 v142, 1.0, v142
	v_add_f32_e32 v143, 1.0, v143
	v_add_f32_e32 v144, 1.0, v144
	v_add_f32_e32 v145, 1.0, v145
	v_add_f32_e32 v146, 1.0, v146
	v_add_f32_e32 v147, 1.0, v147
	v_add_f32_e32 v148, 1.0, v148
	v_add_f32_e32 v149, 1.0, v149
	v_rcp_f32_e32 v134, v134
	v_rcp_f32_e32 v135, v135
	v_rcp_f32_e32 v136, v136
	v_rcp_f32_e32 v137, v137
	v_rcp_f32_e32 v138, v138
	v_rcp_f32_e32 v139, v139
	v_rcp_f32_e32 v140, v140
	v_rcp_f32_e32 v141, v141
	v_rcp_f32_e32 v142, v142
	v_rcp_f32_e32 v143, v143
	v_rcp_f32_e32 v144, v144
	v_rcp_f32_e32 v145, v145
	v_rcp_f32_e32 v146, v146
	v_rcp_f32_e32 v147, v147
	v_rcp_f32_e32 v148, v148
	v_rcp_f32_e32 v149, v149
	v_pk_mul_f32 v[114:115], v[114:115], v[134:135]
	v_pk_mul_f32 v[116:117], v[116:117], v[136:137]
	v_pk_mul_f32 v[106:107], v[106:107], v[138:139]
	v_pk_mul_f32 v[108:109], v[108:109], v[140:141]
	v_pk_mul_f32 v[98:99], v[98:99], v[142:143]
	v_pk_mul_f32 v[100:101], v[100:101], v[144:145]
	v_pk_mul_f32 v[86:87], v[86:87], v[146:147]
	v_pk_mul_f32 v[88:89], v[88:89], v[148:149]
	v_pk_mul_f32 v[114:115], v[130:131], v[114:115]
	v_pk_mul_f32 v[116:117], v[132:133], v[116:117]
	v_pk_mul_f32 v[106:107], v[126:127], v[106:107]
	v_pk_mul_f32 v[108:109], v[128:129], v[108:109]
	v_pk_mul_f32 v[98:99], v[122:123], v[98:99]
	v_pk_mul_f32 v[100:101], v[124:125], v[100:101]
	v_pk_mul_f32 v[86:87], v[118:119], v[86:87]
	v_pk_mul_f32 v[88:89], v[120:121], v[88:89]
	v_cvt_pk_f16_f32 v150, v114, v115
	v_cvt_pk_f16_f32 v151, v116, v117
	v_cvt_pk_f16_f32 v152, v106, v107
	v_cvt_pk_f16_f32 v153, v108, v109
	v_cvt_pk_f16_f32 v154, v98, v99
	v_cvt_pk_f16_f32 v155, v100, v101
	v_cvt_pk_f16_f32 v156, v86, v87
	v_cvt_pk_f16_f32 v157, v88, v89
	global_store_dwordx4 v182, v[150:153], s[42:43]
	global_store_dwordx4 v183, v[154:157], s[42:43]
	v_mul_f32_e32 v134, 0xbfb8aa3b, v74
	v_mul_f32_e32 v135, 0xbfb8aa3b, v75
	v_mul_f32_e32 v136, 0xbfb8aa3b, v76
	v_mul_f32_e32 v137, 0xbfb8aa3b, v77
	v_mul_f32_e32 v138, 0xbfb8aa3b, v62
	v_mul_f32_e32 v139, 0xbfb8aa3b, v63
	v_mul_f32_e32 v140, 0xbfb8aa3b, v64
	v_mul_f32_e32 v141, 0xbfb8aa3b, v65
	v_mul_f32_e32 v142, 0xbfb8aa3b, v46
	v_mul_f32_e32 v143, 0xbfb8aa3b, v47
	v_mul_f32_e32 v144, 0xbfb8aa3b, v48
	v_mul_f32_e32 v145, 0xbfb8aa3b, v49
	v_mul_f32_e32 v146, 0xbfb8aa3b, v34
	v_mul_f32_e32 v147, 0xbfb8aa3b, v35
	v_mul_f32_e32 v148, 0xbfb8aa3b, v36
	v_mul_f32_e32 v149, 0xbfb8aa3b, v37
	v_exp_f32_e32 v134, v134
	v_exp_f32_e32 v135, v135
	v_exp_f32_e32 v136, v136
	v_exp_f32_e32 v137, v137
	v_exp_f32_e32 v138, v138
	v_exp_f32_e32 v139, v139
	v_exp_f32_e32 v140, v140
	v_exp_f32_e32 v141, v141
	v_exp_f32_e32 v142, v142
	v_exp_f32_e32 v143, v143
	v_exp_f32_e32 v144, v144
	v_exp_f32_e32 v145, v145
	v_exp_f32_e32 v146, v146
	v_exp_f32_e32 v147, v147
	v_exp_f32_e32 v148, v148
	v_exp_f32_e32 v149, v149
	v_add_f32_e32 v134, 1.0, v134
	v_add_f32_e32 v135, 1.0, v135
	v_add_f32_e32 v136, 1.0, v136
	v_add_f32_e32 v137, 1.0, v137
	v_add_f32_e32 v138, 1.0, v138
	v_add_f32_e32 v139, 1.0, v139
	v_add_f32_e32 v140, 1.0, v140
	v_add_f32_e32 v141, 1.0, v141
	v_add_f32_e32 v142, 1.0, v142
	v_add_f32_e32 v143, 1.0, v143
	v_add_f32_e32 v144, 1.0, v144
	v_add_f32_e32 v145, 1.0, v145
	v_add_f32_e32 v146, 1.0, v146
	v_add_f32_e32 v147, 1.0, v147
	v_add_f32_e32 v148, 1.0, v148
	v_add_f32_e32 v149, 1.0, v149
	v_rcp_f32_e32 v134, v134
	v_rcp_f32_e32 v135, v135
	v_rcp_f32_e32 v136, v136
	v_rcp_f32_e32 v137, v137
	v_rcp_f32_e32 v138, v138
	v_rcp_f32_e32 v139, v139
	v_rcp_f32_e32 v140, v140
	v_rcp_f32_e32 v141, v141
	v_rcp_f32_e32 v142, v142
	v_rcp_f32_e32 v143, v143
	v_rcp_f32_e32 v144, v144
	v_rcp_f32_e32 v145, v145
	v_rcp_f32_e32 v146, v146
	v_rcp_f32_e32 v147, v147
	v_rcp_f32_e32 v148, v148
	v_rcp_f32_e32 v149, v149
	v_pk_mul_f32 v[74:75], v[74:75], v[134:135]
	v_pk_mul_f32 v[76:77], v[76:77], v[136:137]
	v_pk_mul_f32 v[62:63], v[62:63], v[138:139]
	v_pk_mul_f32 v[64:65], v[64:65], v[140:141]
	v_pk_mul_f32 v[46:47], v[46:47], v[142:143]
	v_pk_mul_f32 v[48:49], v[48:49], v[144:145]
	v_pk_mul_f32 v[34:35], v[34:35], v[146:147]
	v_pk_mul_f32 v[36:37], v[36:37], v[148:149]
	v_pk_mul_f32 v[74:75], v[110:111], v[74:75]
	v_pk_mul_f32 v[76:77], v[112:113], v[76:77]
	v_pk_mul_f32 v[62:63], v[102:103], v[62:63]
	v_pk_mul_f32 v[64:65], v[104:105], v[64:65]
	v_pk_mul_f32 v[46:47], v[94:95], v[46:47]
	v_pk_mul_f32 v[48:49], v[96:97], v[48:49]
	v_pk_mul_f32 v[34:35], v[82:83], v[34:35]
	v_pk_mul_f32 v[36:37], v[84:85], v[36:37]
	v_cvt_pk_f16_f32 v158, v74, v75
	v_cvt_pk_f16_f32 v159, v76, v77
	v_cvt_pk_f16_f32 v160, v62, v63
	v_cvt_pk_f16_f32 v161, v64, v65
	v_cvt_pk_f16_f32 v162, v46, v47
	v_cvt_pk_f16_f32 v163, v48, v49
	v_cvt_pk_f16_f32 v164, v34, v35
	v_cvt_pk_f16_f32 v165, v36, v37
	global_store_dwordx4 v184, v[158:161], s[42:43]
	global_store_dwordx4 v185, v[162:165], s[42:43]
	v_mul_f32_e32 v134, 0xbfb8aa3b, v70
	v_mul_f32_e32 v135, 0xbfb8aa3b, v71
	v_mul_f32_e32 v136, 0xbfb8aa3b, v72
	v_mul_f32_e32 v137, 0xbfb8aa3b, v73
	v_mul_f32_e32 v138, 0xbfb8aa3b, v58
	v_mul_f32_e32 v139, 0xbfb8aa3b, v59
	v_mul_f32_e32 v140, 0xbfb8aa3b, v60
	v_mul_f32_e32 v141, 0xbfb8aa3b, v61
	v_mul_f32_e32 v142, 0xbfb8aa3b, v50
	v_mul_f32_e32 v143, 0xbfb8aa3b, v51
	v_mul_f32_e32 v144, 0xbfb8aa3b, v52
	v_mul_f32_e32 v145, 0xbfb8aa3b, v53
	v_mul_f32_e32 v146, 0xbfb8aa3b, v38
	v_mul_f32_e32 v147, 0xbfb8aa3b, v39
	v_mul_f32_e32 v148, 0xbfb8aa3b, v40
	v_mul_f32_e32 v149, 0xbfb8aa3b, v41
	v_exp_f32_e32 v134, v134
	v_exp_f32_e32 v135, v135
	v_exp_f32_e32 v136, v136
	v_exp_f32_e32 v137, v137
	v_exp_f32_e32 v138, v138
	v_exp_f32_e32 v139, v139
	v_exp_f32_e32 v140, v140
	v_exp_f32_e32 v141, v141
	v_exp_f32_e32 v142, v142
	v_exp_f32_e32 v143, v143
	v_exp_f32_e32 v144, v144
	v_exp_f32_e32 v145, v145
	v_exp_f32_e32 v146, v146
	v_exp_f32_e32 v147, v147
	v_exp_f32_e32 v148, v148
	v_exp_f32_e32 v149, v149
	v_add_f32_e32 v134, 1.0, v134
	v_add_f32_e32 v135, 1.0, v135
	v_add_f32_e32 v136, 1.0, v136
	v_add_f32_e32 v137, 1.0, v137
	v_add_f32_e32 v138, 1.0, v138
	v_add_f32_e32 v139, 1.0, v139
	v_add_f32_e32 v140, 1.0, v140
	v_add_f32_e32 v141, 1.0, v141
	v_add_f32_e32 v142, 1.0, v142
	v_add_f32_e32 v143, 1.0, v143
	v_add_f32_e32 v144, 1.0, v144
	v_add_f32_e32 v145, 1.0, v145
	v_add_f32_e32 v146, 1.0, v146
	v_add_f32_e32 v147, 1.0, v147
	v_add_f32_e32 v148, 1.0, v148
	v_add_f32_e32 v149, 1.0, v149
	v_rcp_f32_e32 v134, v134
	v_rcp_f32_e32 v135, v135
	v_rcp_f32_e32 v136, v136
	v_rcp_f32_e32 v137, v137
	v_rcp_f32_e32 v138, v138
	v_rcp_f32_e32 v139, v139
	v_rcp_f32_e32 v140, v140
	v_rcp_f32_e32 v141, v141
	v_rcp_f32_e32 v142, v142
	v_rcp_f32_e32 v143, v143
	v_rcp_f32_e32 v144, v144
	v_rcp_f32_e32 v145, v145
	v_rcp_f32_e32 v146, v146
	v_rcp_f32_e32 v147, v147
	v_rcp_f32_e32 v148, v148
	v_rcp_f32_e32 v149, v149
	v_pk_mul_f32 v[70:71], v[70:71], v[134:135]
	v_pk_mul_f32 v[72:73], v[72:73], v[136:137]
	v_pk_mul_f32 v[58:59], v[58:59], v[138:139]
	v_pk_mul_f32 v[60:61], v[60:61], v[140:141]
	v_pk_mul_f32 v[50:51], v[50:51], v[142:143]
	v_pk_mul_f32 v[52:53], v[52:53], v[144:145]
	v_pk_mul_f32 v[38:39], v[38:39], v[146:147]
	v_pk_mul_f32 v[40:41], v[40:41], v[148:149]
	v_pk_mul_f32 v[70:71], v[90:91], v[70:71]
	v_pk_mul_f32 v[72:73], v[92:93], v[72:73]
	v_pk_mul_f32 v[58:59], v[78:79], v[58:59]
	v_pk_mul_f32 v[60:61], v[80:81], v[60:61]
	v_pk_mul_f32 v[50:51], v[66:67], v[50:51]
	v_pk_mul_f32 v[52:53], v[68:69], v[52:53]
	v_pk_mul_f32 v[38:39], v[54:55], v[38:39]
	v_pk_mul_f32 v[40:41], v[56:57], v[40:41]
	v_cvt_pk_f16_f32 v166, v70, v71
	v_cvt_pk_f16_f32 v167, v72, v73
	v_cvt_pk_f16_f32 v168, v58, v59
	v_cvt_pk_f16_f32 v169, v60, v61
	v_cvt_pk_f16_f32 v170, v50, v51
	v_cvt_pk_f16_f32 v171, v52, v53
	v_cvt_pk_f16_f32 v172, v38, v39
	v_cvt_pk_f16_f32 v173, v40, v41
	global_store_dwordx4 v182, v[166:169], s[94:95]
	global_store_dwordx4 v183, v[170:173], s[94:95]
	v_mul_f32_e32 v134, 0xbfb8aa3b, v26
	v_mul_f32_e32 v135, 0xbfb8aa3b, v27
	v_mul_f32_e32 v136, 0xbfb8aa3b, v28
	v_mul_f32_e32 v137, 0xbfb8aa3b, v29
	v_mul_f32_e32 v138, 0xbfb8aa3b, v18
	v_mul_f32_e32 v139, 0xbfb8aa3b, v19
	v_mul_f32_e32 v140, 0xbfb8aa3b, v20
	v_mul_f32_e32 v141, 0xbfb8aa3b, v21
	v_mul_f32_e32 v142, 0xbfb8aa3b, v10
	v_mul_f32_e32 v143, 0xbfb8aa3b, v11
	v_mul_f32_e32 v144, 0xbfb8aa3b, v12
	v_mul_f32_e32 v145, 0xbfb8aa3b, v13
	v_mul_f32_e32 v146, 0xbfb8aa3b, v6
	v_mul_f32_e32 v147, 0xbfb8aa3b, v7
	v_mul_f32_e32 v148, 0xbfb8aa3b, v8
	v_mul_f32_e32 v149, 0xbfb8aa3b, v9
	v_exp_f32_e32 v134, v134
	v_exp_f32_e32 v135, v135
	v_exp_f32_e32 v136, v136
	v_exp_f32_e32 v137, v137
	v_exp_f32_e32 v138, v138
	v_exp_f32_e32 v139, v139
	v_exp_f32_e32 v140, v140
	v_exp_f32_e32 v141, v141
	v_exp_f32_e32 v142, v142
	v_exp_f32_e32 v143, v143
	v_exp_f32_e32 v144, v144
	v_exp_f32_e32 v145, v145
	v_exp_f32_e32 v146, v146
	v_exp_f32_e32 v147, v147
	v_exp_f32_e32 v148, v148
	v_exp_f32_e32 v149, v149
	v_add_f32_e32 v134, 1.0, v134
	v_add_f32_e32 v135, 1.0, v135
	v_add_f32_e32 v136, 1.0, v136
	v_add_f32_e32 v137, 1.0, v137
	v_add_f32_e32 v138, 1.0, v138
	v_add_f32_e32 v139, 1.0, v139
	v_add_f32_e32 v140, 1.0, v140
	v_add_f32_e32 v141, 1.0, v141
	v_add_f32_e32 v142, 1.0, v142
	v_add_f32_e32 v143, 1.0, v143
	v_add_f32_e32 v144, 1.0, v144
	v_add_f32_e32 v145, 1.0, v145
	v_add_f32_e32 v146, 1.0, v146
	v_add_f32_e32 v147, 1.0, v147
	v_add_f32_e32 v148, 1.0, v148
	v_add_f32_e32 v149, 1.0, v149
	v_rcp_f32_e32 v134, v134
	v_rcp_f32_e32 v135, v135
	v_rcp_f32_e32 v136, v136
	v_rcp_f32_e32 v137, v137
	v_rcp_f32_e32 v138, v138
	v_rcp_f32_e32 v139, v139
	v_rcp_f32_e32 v140, v140
	v_rcp_f32_e32 v141, v141
	v_rcp_f32_e32 v142, v142
	v_rcp_f32_e32 v143, v143
	v_rcp_f32_e32 v144, v144
	v_rcp_f32_e32 v145, v145
	v_rcp_f32_e32 v146, v146
	v_rcp_f32_e32 v147, v147
	v_rcp_f32_e32 v148, v148
	v_rcp_f32_e32 v149, v149
	v_pk_mul_f32 v[26:27], v[26:27], v[134:135]
	v_pk_mul_f32 v[28:29], v[28:29], v[136:137]
	v_pk_mul_f32 v[18:19], v[18:19], v[138:139]
	v_pk_mul_f32 v[20:21], v[20:21], v[140:141]
	v_pk_mul_f32 v[10:11], v[10:11], v[142:143]
	v_pk_mul_f32 v[12:13], v[12:13], v[144:145]
	v_pk_mul_f32 v[6:7], v[6:7], v[146:147]
	v_pk_mul_f32 v[8:9], v[8:9], v[148:149]
	v_pk_mul_f32 v[26:27], v[42:43], v[26:27]
	v_pk_mul_f32 v[28:29], v[44:45], v[28:29]
	v_pk_mul_f32 v[18:19], v[30:31], v[18:19]
	v_pk_mul_f32 v[20:21], v[32:33], v[20:21]
	v_pk_mul_f32 v[10:11], v[22:23], v[10:11]
	v_pk_mul_f32 v[12:13], v[24:25], v[12:13]
	v_pk_mul_f32 v[6:7], v[14:15], v[6:7]
	v_pk_mul_f32 v[8:9], v[16:17], v[8:9]
	v_cvt_pk_f16_f32 v174, v26, v27
	v_cvt_pk_f16_f32 v175, v28, v29
	v_cvt_pk_f16_f32 v176, v18, v19
	v_cvt_pk_f16_f32 v177, v20, v21
	v_cvt_pk_f16_f32 v178, v10, v11
	v_cvt_pk_f16_f32 v179, v12, v13
	v_cvt_pk_f16_f32 v180, v6, v7
	v_cvt_pk_f16_f32 v181, v8, v9
	global_store_dwordx4 v184, v[174:177], s[94:95]
	global_store_dwordx4 v185, v[178:181], s[94:95]
	s_cbranch_vccnz .LBB4_51
	s_mov_b32 s83, s80
	s_mov_b32 s81, s78
	s_mov_b32 s82, s79
	s_mov_b64 s[44:45], s[40:41]
	s_mov_b64 s[46:47], s[38:39]
	s_branch .LBB4_11

	.amdhsa_kernel _Z7k_gemm1ILi0EEvPKDF16_S1_PDF16_PK15HIP_vector_typeIiLj2EEPKfS8_S2_PKt
		.amdhsa_group_segment_fixed_size 0
		.amdhsa_private_segment_fixed_size 0
		.amdhsa_kernarg_size 64
		.amdhsa_user_sgpr_count 2
		.amdhsa_user_sgpr_dispatch_ptr 0
		.amdhsa_user_sgpr_queue_ptr 0
		.amdhsa_user_sgpr_kernarg_segment_ptr 1
		.amdhsa_user_sgpr_dispatch_id 0
		.amdhsa_user_sgpr_kernarg_preload_length 0
		.amdhsa_user_sgpr_kernarg_preload_offset 0
		.amdhsa_user_sgpr_private_segment_size 0
		.amdhsa_uses_dynamic_stack 0
		.amdhsa_enable_private_segment 0
		.amdhsa_system_sgpr_workgroup_id_x 1
		.amdhsa_system_sgpr_workgroup_id_y 0
		.amdhsa_system_sgpr_workgroup_id_z 0
		.amdhsa_system_sgpr_workgroup_info 0
		.amdhsa_system_vgpr_workitem_id 0
		.amdhsa_next_free_vgpr 256
		.amdhsa_next_free_sgpr 96
		.amdhsa_accum_offset 256
		.amdhsa_reserve_vcc 1
		.amdhsa_float_round_mode_32 0
		.amdhsa_float_round_mode_16_64 0
		.amdhsa_float_denorm_mode_32 3
		.amdhsa_float_denorm_mode_16_64 3
		.amdhsa_dx10_clamp 1
		.amdhsa_ieee_mode 1
		.amdhsa_fp16_overflow 0
		.amdhsa_tg_split 0
		.amdhsa_exception_fp_ieee_invalid_op 0
		.amdhsa_exception_fp_denorm_src 0
		.amdhsa_exception_fp_ieee_div_zero 0
		.amdhsa_exception_fp_ieee_overflow 0
		.amdhsa_exception_fp_ieee_underflow 0
		.amdhsa_exception_fp_ieee_inexact 0
		.amdhsa_exception_int_div_zero 0
	.end_amdhsa_kernel

.LBB5_49:
	s_mov_b64 vcc, s[0:1]
	s_lshl_b32 s29, s78, 8
	s_add_i32 s29, s29, s60
	s_lshl_b32 s24, s77, 7
	s_or_b32 s24, s24, s61
	s_ashr_i32 s31, s29, 8
	s_ashr_i32 s24, s24, 6
	s_mul_i32 s31, s31, 44
	s_add_i32 s31, s31, s24
	s_lshl_b32 s31, s31, 1
	v_or_b32_e32 v188, s29, v230
	s_or_b32 s38, s31, s69
	s_ashr_i32 s39, s38, 31
	v_lshlrev_b32_e32 v189, 6, v188
	s_lshl_b64 s[38:39], s[38:39], 14
	v_and_or_b32 v186, v189, s67, v231
	v_lshlrev_b32_e32 v189, 2, v188
	v_and_b32_e32 v187, 32, v189
	s_add_u32 s38, s2, s38
	s_addc_u32 s39, s3, s39
	v_bitop3_b32 v182, v186, s70, v187 bitop3:0xde
	s_or_b32 s31, s29, 16
	s_lshr_b32 s31, s31, 3
	s_and_b32 s31, s31, 10
	s_or_b32 s31, s31, s68
	s_lshl_b32 s31, s31, 10
	v_bitop3_b32 v183, v186, s31, v187 bitop3:0xde
	s_or_b32 s31, s29, 32
	s_lshr_b32 s31, s31, 3
	s_and_b32 s31, s31, 12
	s_or_b32 s31, s31, s68
	s_lshl_b32 s31, s31, 10
	v_bitop3_b32 v184, v186, s31, v187 bitop3:0xde
	s_or_b32 s29, s29, 48
	s_lshr_b32 s29, s29, 3
	s_and_b32 s29, s29, 14
	s_or_b32 s29, s29, s68
	s_lshl_b32 s29, s29, 10
	v_bitop3_b32 v185, v186, s29, v187 bitop3:0xde
	s_add_u32 s88, s38, 0x4000
	s_addc_u32 s89, s39, 0
	v_mul_f32_e32 v134, 0xbfb8aa3b, v118
	v_mul_f32_e32 v135, 0xbfb8aa3b, v119
	v_mul_f32_e32 v136, 0xbfb8aa3b, v120
	v_mul_f32_e32 v137, 0xbfb8aa3b, v121
	v_mul_f32_e32 v138, 0xbfb8aa3b, v110
	v_mul_f32_e32 v139, 0xbfb8aa3b, v111
	v_mul_f32_e32 v140, 0xbfb8aa3b, v112
	v_mul_f32_e32 v141, 0xbfb8aa3b, v113
	v_mul_f32_e32 v142, 0xbfb8aa3b, v102
	v_mul_f32_e32 v143, 0xbfb8aa3b, v103
	v_mul_f32_e32 v144, 0xbfb8aa3b, v104
	v_mul_f32_e32 v145, 0xbfb8aa3b, v105
	v_mul_f32_e32 v146, 0xbfb8aa3b, v94
	v_mul_f32_e32 v147, 0xbfb8aa3b, v95
	v_mul_f32_e32 v148, 0xbfb8aa3b, v96
	v_mul_f32_e32 v149, 0xbfb8aa3b, v97
	v_exp_f32_e32 v134, v134
	v_exp_f32_e32 v135, v135
	v_exp_f32_e32 v136, v136
	v_exp_f32_e32 v137, v137
	v_exp_f32_e32 v138, v138
	v_exp_f32_e32 v139, v139
	v_exp_f32_e32 v140, v140
	v_exp_f32_e32 v141, v141
	v_exp_f32_e32 v142, v142
	v_exp_f32_e32 v143, v143
	v_exp_f32_e32 v144, v144
	v_exp_f32_e32 v145, v145
	v_exp_f32_e32 v146, v146
	v_exp_f32_e32 v147, v147
	v_exp_f32_e32 v148, v148
	v_exp_f32_e32 v149, v149
	v_add_f32_e32 v134, 1.0, v134
	v_add_f32_e32 v135, 1.0, v135
	v_add_f32_e32 v136, 1.0, v136
	v_add_f32_e32 v137, 1.0, v137
	v_add_f32_e32 v138, 1.0, v138
	v_add_f32_e32 v139, 1.0, v139
	v_add_f32_e32 v140, 1.0, v140
	v_add_f32_e32 v141, 1.0, v141
	v_add_f32_e32 v142, 1.0, v142
	v_add_f32_e32 v143, 1.0, v143
	v_add_f32_e32 v144, 1.0, v144
	v_add_f32_e32 v145, 1.0, v145
	v_add_f32_e32 v146, 1.0, v146
	v_add_f32_e32 v147, 1.0, v147
	v_add_f32_e32 v148, 1.0, v148
	v_add_f32_e32 v149, 1.0, v149
	v_rcp_f32_e32 v134, v134
	v_rcp_f32_e32 v135, v135
	v_rcp_f32_e32 v136, v136
	v_rcp_f32_e32 v137, v137
	v_rcp_f32_e32 v138, v138
	v_rcp_f32_e32 v139, v139
	v_rcp_f32_e32 v140, v140
	v_rcp_f32_e32 v141, v141
	v_rcp_f32_e32 v142, v142
	v_rcp_f32_e32 v143, v143
	v_rcp_f32_e32 v144, v144
	v_rcp_f32_e32 v145, v145
	v_rcp_f32_e32 v146, v146
	v_rcp_f32_e32 v147, v147
	v_rcp_f32_e32 v148, v148
	v_rcp_f32_e32 v149, v149
	v_pk_mul_f32 v[118:119], v[118:119], v[134:135]
	v_pk_mul_f32 v[120:121], v[120:121], v[136:137]
	v_pk_mul_f32 v[110:111], v[110:111], v[138:139]
	v_pk_mul_f32 v[112:113], v[112:113], v[140:141]
	v_pk_mul_f32 v[102:103], v[102:103], v[142:143]
	v_pk_mul_f32 v[104:105], v[104:105], v[144:145]
	v_pk_mul_f32 v[94:95], v[94:95], v[146:147]
	v_pk_mul_f32 v[96:97], v[96:97], v[148:149]
	v_pk_mul_f32 v[118:119], v[130:131], v[118:119]
	v_pk_mul_f32 v[120:121], v[132:133], v[120:121]
	v_pk_mul_f32 v[110:111], v[126:127], v[110:111]
	v_pk_mul_f32 v[112:113], v[128:129], v[112:113]
	v_pk_mul_f32 v[102:103], v[122:123], v[102:103]
	v_pk_mul_f32 v[104:105], v[124:125], v[104:105]
	v_pk_mul_f32 v[94:95], v[114:115], v[94:95]
	v_pk_mul_f32 v[96:97], v[116:117], v[96:97]
	v_cvt_pk_f16_f32 v150, v118, v119
	v_cvt_pk_f16_f32 v151, v120, v121
	v_cvt_pk_f16_f32 v152, v110, v111
	v_cvt_pk_f16_f32 v153, v112, v113
	v_cvt_pk_f16_f32 v154, v102, v103
	v_cvt_pk_f16_f32 v155, v104, v105
	v_cvt_pk_f16_f32 v156, v94, v95
	v_cvt_pk_f16_f32 v157, v96, v97
	global_store_dwordx4 v182, v[150:153], s[38:39]
	global_store_dwordx4 v183, v[154:157], s[38:39]
	v_mul_f32_e32 v134, 0xbfb8aa3b, v82
	v_mul_f32_e32 v135, 0xbfb8aa3b, v83
	v_mul_f32_e32 v136, 0xbfb8aa3b, v84
	v_mul_f32_e32 v137, 0xbfb8aa3b, v85
	v_mul_f32_e32 v138, 0xbfb8aa3b, v66
	v_mul_f32_e32 v139, 0xbfb8aa3b, v67
	v_mul_f32_e32 v140, 0xbfb8aa3b, v68
	v_mul_f32_e32 v141, 0xbfb8aa3b, v69
	v_mul_f32_e32 v142, 0xbfb8aa3b, v54
	v_mul_f32_e32 v143, 0xbfb8aa3b, v55
	v_mul_f32_e32 v144, 0xbfb8aa3b, v56
	v_mul_f32_e32 v145, 0xbfb8aa3b, v57
	v_mul_f32_e32 v146, 0xbfb8aa3b, v42
	v_mul_f32_e32 v147, 0xbfb8aa3b, v43
	v_mul_f32_e32 v148, 0xbfb8aa3b, v44
	v_mul_f32_e32 v149, 0xbfb8aa3b, v45
	v_exp_f32_e32 v134, v134
	v_exp_f32_e32 v135, v135
	v_exp_f32_e32 v136, v136
	v_exp_f32_e32 v137, v137
	v_exp_f32_e32 v138, v138
	v_exp_f32_e32 v139, v139
	v_exp_f32_e32 v140, v140
	v_exp_f32_e32 v141, v141
	v_exp_f32_e32 v142, v142
	v_exp_f32_e32 v143, v143
	v_exp_f32_e32 v144, v144
	v_exp_f32_e32 v145, v145
	v_exp_f32_e32 v146, v146
	v_exp_f32_e32 v147, v147
	v_exp_f32_e32 v148, v148
	v_exp_f32_e32 v149, v149
	v_add_f32_e32 v134, 1.0, v134
	v_add_f32_e32 v135, 1.0, v135
	v_add_f32_e32 v136, 1.0, v136
	v_add_f32_e32 v137, 1.0, v137
	v_add_f32_e32 v138, 1.0, v138
	v_add_f32_e32 v139, 1.0, v139
	v_add_f32_e32 v140, 1.0, v140
	v_add_f32_e32 v141, 1.0, v141
	v_add_f32_e32 v142, 1.0, v142
	v_add_f32_e32 v143, 1.0, v143
	v_add_f32_e32 v144, 1.0, v144
	v_add_f32_e32 v145, 1.0, v145
	v_add_f32_e32 v146, 1.0, v146
	v_add_f32_e32 v147, 1.0, v147
	v_add_f32_e32 v148, 1.0, v148
	v_add_f32_e32 v149, 1.0, v149
	v_rcp_f32_e32 v134, v134
	v_rcp_f32_e32 v135, v135
	v_rcp_f32_e32 v136, v136
	v_rcp_f32_e32 v137, v137
	v_rcp_f32_e32 v138, v138
	v_rcp_f32_e32 v139, v139
	v_rcp_f32_e32 v140, v140
	v_rcp_f32_e32 v141, v141
	v_rcp_f32_e32 v142, v142
	v_rcp_f32_e32 v143, v143
	v_rcp_f32_e32 v144, v144
	v_rcp_f32_e32 v145, v145
	v_rcp_f32_e32 v146, v146
	v_rcp_f32_e32 v147, v147
	v_rcp_f32_e32 v148, v148
	v_rcp_f32_e32 v149, v149
	v_pk_mul_f32 v[82:83], v[82:83], v[134:135]
	v_pk_mul_f32 v[84:85], v[84:85], v[136:137]
	v_pk_mul_f32 v[66:67], v[66:67], v[138:139]
	v_pk_mul_f32 v[68:69], v[68:69], v[140:141]
	v_pk_mul_f32 v[54:55], v[54:55], v[142:143]
	v_pk_mul_f32 v[56:57], v[56:57], v[144:145]
	v_pk_mul_f32 v[42:43], v[42:43], v[146:147]
	v_pk_mul_f32 v[44:45], v[44:45], v[148:149]
	v_pk_mul_f32 v[82:83], v[106:107], v[82:83]
	v_pk_mul_f32 v[84:85], v[108:109], v[84:85]
	v_pk_mul_f32 v[66:67], v[98:99], v[66:67]
	v_pk_mul_f32 v[68:69], v[100:101], v[68:69]
	v_pk_mul_f32 v[54:55], v[90:91], v[54:55]
	v_pk_mul_f32 v[56:57], v[92:93], v[56:57]
	v_pk_mul_f32 v[42:43], v[78:79], v[42:43]
	v_pk_mul_f32 v[44:45], v[80:81], v[44:45]
	v_cvt_pk_f16_f32 v158, v82, v83
	v_cvt_pk_f16_f32 v159, v84, v85
	v_cvt_pk_f16_f32 v160, v66, v67
	v_cvt_pk_f16_f32 v161, v68, v69
	v_cvt_pk_f16_f32 v162, v54, v55
	v_cvt_pk_f16_f32 v163, v56, v57
	v_cvt_pk_f16_f32 v164, v42, v43
	v_cvt_pk_f16_f32 v165, v44, v45
	global_store_dwordx4 v184, v[158:161], s[38:39]
	global_store_dwordx4 v185, v[162:165], s[38:39]
	v_mul_f32_e32 v134, 0xbfb8aa3b, v70
	v_mul_f32_e32 v135, 0xbfb8aa3b, v71
	v_mul_f32_e32 v136, 0xbfb8aa3b, v72
	v_mul_f32_e32 v137, 0xbfb8aa3b, v73
	v_mul_f32_e32 v138, 0xbfb8aa3b, v58
	v_mul_f32_e32 v139, 0xbfb8aa3b, v59
	v_mul_f32_e32 v140, 0xbfb8aa3b, v60
	v_mul_f32_e32 v141, 0xbfb8aa3b, v61
	v_mul_f32_e32 v142, 0xbfb8aa3b, v46
	v_mul_f32_e32 v143, 0xbfb8aa3b, v47
	v_mul_f32_e32 v144, 0xbfb8aa3b, v48
	v_mul_f32_e32 v145, 0xbfb8aa3b, v49
	v_mul_f32_e32 v146, 0xbfb8aa3b, v34
	v_mul_f32_e32 v147, 0xbfb8aa3b, v35
	v_mul_f32_e32 v148, 0xbfb8aa3b, v36
	v_mul_f32_e32 v149, 0xbfb8aa3b, v37
	v_exp_f32_e32 v134, v134
	v_exp_f32_e32 v135, v135
	v_exp_f32_e32 v136, v136
	v_exp_f32_e32 v137, v137
	v_exp_f32_e32 v138, v138
	v_exp_f32_e32 v139, v139
	v_exp_f32_e32 v140, v140
	v_exp_f32_e32 v141, v141
	v_exp_f32_e32 v142, v142
	v_exp_f32_e32 v143, v143
	v_exp_f32_e32 v144, v144
	v_exp_f32_e32 v145, v145
	v_exp_f32_e32 v146, v146
	v_exp_f32_e32 v147, v147
	v_exp_f32_e32 v148, v148
	v_exp_f32_e32 v149, v149
	v_add_f32_e32 v134, 1.0, v134
	v_add_f32_e32 v135, 1.0, v135
	v_add_f32_e32 v136, 1.0, v136
	v_add_f32_e32 v137, 1.0, v137
	v_add_f32_e32 v138, 1.0, v138
	v_add_f32_e32 v139, 1.0, v139
	v_add_f32_e32 v140, 1.0, v140
	v_add_f32_e32 v141, 1.0, v141
	v_add_f32_e32 v142, 1.0, v142
	v_add_f32_e32 v143, 1.0, v143
	v_add_f32_e32 v144, 1.0, v144
	v_add_f32_e32 v145, 1.0, v145
	v_add_f32_e32 v146, 1.0, v146
	v_add_f32_e32 v147, 1.0, v147
	v_add_f32_e32 v148, 1.0, v148
	v_add_f32_e32 v149, 1.0, v149
	v_rcp_f32_e32 v134, v134
	v_rcp_f32_e32 v135, v135
	v_rcp_f32_e32 v136, v136
	v_rcp_f32_e32 v137, v137
	v_rcp_f32_e32 v138, v138
	v_rcp_f32_e32 v139, v139
	v_rcp_f32_e32 v140, v140
	v_rcp_f32_e32 v141, v141
	v_rcp_f32_e32 v142, v142
	v_rcp_f32_e32 v143, v143
	v_rcp_f32_e32 v144, v144
	v_rcp_f32_e32 v145, v145
	v_rcp_f32_e32 v146, v146
	v_rcp_f32_e32 v147, v147
	v_rcp_f32_e32 v148, v148
	v_rcp_f32_e32 v149, v149
	v_pk_mul_f32 v[70:71], v[70:71], v[134:135]
	v_pk_mul_f32 v[72:73], v[72:73], v[136:137]
	v_pk_mul_f32 v[58:59], v[58:59], v[138:139]
	v_pk_mul_f32 v[60:61], v[60:61], v[140:141]
	v_pk_mul_f32 v[46:47], v[46:47], v[142:143]
	v_pk_mul_f32 v[48:49], v[48:49], v[144:145]
	v_pk_mul_f32 v[34:35], v[34:35], v[146:147]
	v_pk_mul_f32 v[36:37], v[36:37], v[148:149]
	v_pk_mul_f32 v[70:71], v[86:87], v[70:71]
	v_pk_mul_f32 v[72:73], v[88:89], v[72:73]
	v_pk_mul_f32 v[58:59], v[74:75], v[58:59]
	v_pk_mul_f32 v[60:61], v[76:77], v[60:61]
	v_pk_mul_f32 v[46:47], v[62:63], v[46:47]
	v_pk_mul_f32 v[48:49], v[64:65], v[48:49]
	v_pk_mul_f32 v[34:35], v[50:51], v[34:35]
	v_pk_mul_f32 v[36:37], v[52:53], v[36:37]
	v_cvt_pk_f16_f32 v166, v70, v71
	v_cvt_pk_f16_f32 v167, v72, v73
	v_cvt_pk_f16_f32 v168, v58, v59
	v_cvt_pk_f16_f32 v169, v60, v61
	v_cvt_pk_f16_f32 v170, v46, v47
	v_cvt_pk_f16_f32 v171, v48, v49
	v_cvt_pk_f16_f32 v172, v34, v35
	v_cvt_pk_f16_f32 v173, v36, v37
	global_store_dwordx4 v182, v[166:169], s[88:89]
	global_store_dwordx4 v183, v[170:173], s[88:89]
	v_mul_f32_e32 v134, 0xbfb8aa3b, v26
	v_mul_f32_e32 v135, 0xbfb8aa3b, v27
	v_mul_f32_e32 v136, 0xbfb8aa3b, v28
	v_mul_f32_e32 v137, 0xbfb8aa3b, v29
	v_mul_f32_e32 v138, 0xbfb8aa3b, v18
	v_mul_f32_e32 v139, 0xbfb8aa3b, v19
	v_mul_f32_e32 v140, 0xbfb8aa3b, v20
	v_mul_f32_e32 v141, 0xbfb8aa3b, v21
	v_mul_f32_e32 v142, 0xbfb8aa3b, v10
	v_mul_f32_e32 v143, 0xbfb8aa3b, v11
	v_mul_f32_e32 v144, 0xbfb8aa3b, v12
	v_mul_f32_e32 v145, 0xbfb8aa3b, v13
	v_mul_f32_e32 v146, 0xbfb8aa3b, v6
	v_mul_f32_e32 v147, 0xbfb8aa3b, v7
	v_mul_f32_e32 v148, 0xbfb8aa3b, v8
	v_mul_f32_e32 v149, 0xbfb8aa3b, v9
	v_exp_f32_e32 v134, v134
	v_exp_f32_e32 v135, v135
	v_exp_f32_e32 v136, v136
	v_exp_f32_e32 v137, v137
	v_exp_f32_e32 v138, v138
	v_exp_f32_e32 v139, v139
	v_exp_f32_e32 v140, v140
	v_exp_f32_e32 v141, v141
	v_exp_f32_e32 v142, v142
	v_exp_f32_e32 v143, v143
	v_exp_f32_e32 v144, v144
	v_exp_f32_e32 v145, v145
	v_exp_f32_e32 v146, v146
	v_exp_f32_e32 v147, v147
	v_exp_f32_e32 v148, v148
	v_exp_f32_e32 v149, v149
	v_add_f32_e32 v134, 1.0, v134
	v_add_f32_e32 v135, 1.0, v135
	v_add_f32_e32 v136, 1.0, v136
	v_add_f32_e32 v137, 1.0, v137
	v_add_f32_e32 v138, 1.0, v138
	v_add_f32_e32 v139, 1.0, v139
	v_add_f32_e32 v140, 1.0, v140
	v_add_f32_e32 v141, 1.0, v141
	v_add_f32_e32 v142, 1.0, v142
	v_add_f32_e32 v143, 1.0, v143
	v_add_f32_e32 v144, 1.0, v144
	v_add_f32_e32 v145, 1.0, v145
	v_add_f32_e32 v146, 1.0, v146
	v_add_f32_e32 v147, 1.0, v147
	v_add_f32_e32 v148, 1.0, v148
	v_add_f32_e32 v149, 1.0, v149
	v_rcp_f32_e32 v134, v134
	v_rcp_f32_e32 v135, v135
	v_rcp_f32_e32 v136, v136
	v_rcp_f32_e32 v137, v137
	v_rcp_f32_e32 v138, v138
	v_rcp_f32_e32 v139, v139
	v_rcp_f32_e32 v140, v140
	v_rcp_f32_e32 v141, v141
	v_rcp_f32_e32 v142, v142
	v_rcp_f32_e32 v143, v143
	v_rcp_f32_e32 v144, v144
	v_rcp_f32_e32 v145, v145
	v_rcp_f32_e32 v146, v146
	v_rcp_f32_e32 v147, v147
	v_rcp_f32_e32 v148, v148
	v_rcp_f32_e32 v149, v149
	v_pk_mul_f32 v[26:27], v[26:27], v[134:135]
	v_pk_mul_f32 v[28:29], v[28:29], v[136:137]
	v_pk_mul_f32 v[18:19], v[18:19], v[138:139]
	v_pk_mul_f32 v[20:21], v[20:21], v[140:141]
	v_pk_mul_f32 v[10:11], v[10:11], v[142:143]
	v_pk_mul_f32 v[12:13], v[12:13], v[144:145]
	v_pk_mul_f32 v[6:7], v[6:7], v[146:147]
	v_pk_mul_f32 v[8:9], v[8:9], v[148:149]
	v_pk_mul_f32 v[26:27], v[38:39], v[26:27]
	v_pk_mul_f32 v[28:29], v[40:41], v[28:29]
	v_pk_mul_f32 v[18:19], v[30:31], v[18:19]
	v_pk_mul_f32 v[20:21], v[32:33], v[20:21]
	v_pk_mul_f32 v[10:11], v[22:23], v[10:11]
	v_pk_mul_f32 v[12:13], v[24:25], v[12:13]
	v_pk_mul_f32 v[6:7], v[14:15], v[6:7]
	v_pk_mul_f32 v[8:9], v[16:17], v[8:9]
	v_cvt_pk_f16_f32 v174, v26, v27
	v_cvt_pk_f16_f32 v175, v28, v29
	v_cvt_pk_f16_f32 v176, v18, v19
	v_cvt_pk_f16_f32 v177, v20, v21
	v_cvt_pk_f16_f32 v178, v10, v11
	v_cvt_pk_f16_f32 v179, v12, v13
	v_cvt_pk_f16_f32 v180, v6, v7
	v_cvt_pk_f16_f32 v181, v8, v9
	global_store_dwordx4 v184, v[174:177], s[88:89]
	global_store_dwordx4 v185, v[178:181], s[88:89]
	s_cbranch_vccnz .LBB5_51
	s_mov_b32 s79, s76
	s_mov_b32 s77, s74
	s_mov_b32 s78, s75
	s_mov_b64 s[40:41], s[36:37]
	s_mov_b64 s[42:43], s[34:35]
	s_branch .LBB5_11

	.amdhsa_kernel _Z7k_gemm1ILi1EEvPKDF16_S1_PDF16_PK15HIP_vector_typeIiLj2EEPKfS8_S2_PKt
		.amdhsa_group_segment_fixed_size 0
		.amdhsa_private_segment_fixed_size 0
		.amdhsa_kernarg_size 64
		.amdhsa_user_sgpr_count 2
		.amdhsa_user_sgpr_dispatch_ptr 0
		.amdhsa_user_sgpr_queue_ptr 0
		.amdhsa_user_sgpr_kernarg_segment_ptr 1
		.amdhsa_user_sgpr_dispatch_id 0
		.amdhsa_user_sgpr_kernarg_preload_length 0
		.amdhsa_user_sgpr_kernarg_preload_offset 0
		.amdhsa_user_sgpr_private_segment_size 0
		.amdhsa_uses_dynamic_stack 0
		.amdhsa_enable_private_segment 0
		.amdhsa_system_sgpr_workgroup_id_x 1
		.amdhsa_system_sgpr_workgroup_id_y 0
		.amdhsa_system_sgpr_workgroup_id_z 0
		.amdhsa_system_sgpr_workgroup_info 0
		.amdhsa_system_vgpr_workitem_id 0
		.amdhsa_next_free_vgpr 254
		.amdhsa_next_free_sgpr 90
		.amdhsa_accum_offset 256
		.amdhsa_reserve_vcc 1
		.amdhsa_float_round_mode_32 0
		.amdhsa_float_round_mode_16_64 0
		.amdhsa_float_denorm_mode_32 3
		.amdhsa_float_denorm_mode_16_64 3
		.amdhsa_dx10_clamp 1
		.amdhsa_ieee_mode 1
		.amdhsa_fp16_overflow 0
		.amdhsa_tg_split 0
		.amdhsa_exception_fp_ieee_invalid_op 0
		.amdhsa_exception_fp_denorm_src 0
		.amdhsa_exception_fp_ieee_div_zero 0
		.amdhsa_exception_fp_ieee_overflow 0
		.amdhsa_exception_fp_ieee_underflow 0
		.amdhsa_exception_fp_ieee_inexact 0
		.amdhsa_exception_int_div_zero 0
	.end_amdhsa_kernel

amdhsa.kernels:
  - .agpr_count:     0
    .args:
      - .actual_access:  read_only
        .address_space:  global
        .offset:         0
        .size:           8
        .value_kind:     global_buffer
      - .actual_access:  read_only
        .address_space:  global
        .offset:         8
        .size:           8
        .value_kind:     global_buffer
      - .actual_access:  write_only
        .address_space:  global
        .offset:         16
        .size:           8
        .value_kind:     global_buffer
      - .actual_access:  write_only
        .address_space:  global
        .offset:         24
        .size:           8
        .value_kind:     global_buffer
      - .actual_access:  write_only
        .address_space:  global
        .offset:         32
        .size:           8
        .value_kind:     global_buffer
      - .actual_access:  write_only
        .address_space:  global
        .offset:         40
        .size:           8
        .value_kind:     global_buffer
    .group_segment_fixed_size: 256
    .kernarg_segment_align: 8
    .kernarg_segment_size: 48
    .language:       OpenCL C
    .language_version:
      - 2
      - 0
    .max_flat_workgroup_size: 256
    .name:           _Z10k_xscatterPKiS0_P15HIP_vector_typeIiLj2EEPtP4MetaS3_
    .private_segment_fixed_size: 0
    .sgpr_count:     41
    .sgpr_spill_count: 0
    .symbol:         _Z10k_xscatterPKiS0_P15HIP_vector_typeIiLj2EEPtP4MetaS3_.kd
    .uniform_work_group_size: 1
    .uses_dynamic_stack: false
    .vgpr_count:     55
    .vgpr_spill_count: 0
    .wavefront_size: 64
  - .agpr_count:     0
    .args:
      - .actual_access:  read_only
        .address_space:  global
        .offset:         0
        .size:           8
        .value_kind:     global_buffer
      - .actual_access:  read_only
        .address_space:  global
        .offset:         8
        .size:           8
        .value_kind:     global_buffer
      - .actual_access:  write_only
        .address_space:  global
        .offset:         16
        .size:           8
        .value_kind:     global_buffer
      - .actual_access:  write_only
        .address_space:  global
        .offset:         24
        .size:           8
        .value_kind:     global_buffer
      - .actual_access:  write_only
        .address_space:  global
        .offset:         32
        .size:           8
        .value_kind:     global_buffer
      - .actual_access:  read_only
        .address_space:  global
        .offset:         40
        .size:           8
        .value_kind:     global_buffer
      - .actual_access:  read_only
        .address_space:  global
        .offset:         48
        .size:           8
        .value_kind:     global_buffer
      - .actual_access:  write_only
        .address_space:  global
        .offset:         56
        .size:           8
        .value_kind:     global_buffer
      - .actual_access:  write_only
        .address_space:  global
        .offset:         64
        .size:           8
        .value_kind:     global_buffer
    .group_segment_fixed_size: 4096
    .kernarg_segment_align: 8
    .kernarg_segment_size: 72
    .language:       OpenCL C
    .language_version:
      - 2
      - 0
    .max_flat_workgroup_size: 256
    .name:           _Z5k_prePKfS0_PiP15HIP_vector_typeIfLj2EES1_S0_S0_PDF16_S5_
    .private_segment_fixed_size: 0
    .sgpr_count:     38
    .sgpr_spill_count: 0
    .symbol:         _Z5k_prePKfS0_PiP15HIP_vector_typeIfLj2EES1_S0_S0_PDF16_S5_.kd
    .uniform_work_group_size: 1
    .uses_dynamic_stack: false
    .vgpr_count:     128
    .vgpr_spill_count: 0
    .wavefront_size: 64
  - .agpr_count:     0
    .args:
      - .address_space:  global
        .offset:         0
        .size:           8
        .value_kind:     global_buffer
      - .address_space:  global
        .offset:         8
        .size:           8
        .value_kind:     global_buffer
      - .actual_access:  write_only
        .address_space:  global
        .offset:         16
        .size:           8
        .value_kind:     global_buffer
      - .actual_access:  read_only
        .address_space:  global
        .offset:         24
        .size:           8
        .value_kind:     global_buffer
    .group_segment_fixed_size: 0
    .kernarg_segment_align: 8
    .kernarg_segment_size: 32
    .language:       OpenCL C
    .language_version:
      - 2
      - 0
    .max_flat_workgroup_size: 512
    .name:           _Z7k_gemm2PKDF16_S0_PDF16_PK15HIP_vector_typeIiLj2EE
    .private_segment_fixed_size: 0
    .sgpr_count:     74
    .sgpr_spill_count: 0
    .symbol:         _Z7k_gemm2PKDF16_S0_PDF16_PK15HIP_vector_typeIiLj2EE.kd
    .uniform_work_group_size: 1
    .uses_dynamic_stack: false
    .vgpr_count:     226
    .vgpr_spill_count: 0
    .wavefront_size: 64
  - .agpr_count:     0
    .args:
      - .actual_access:  read_only
        .address_space:  global
        .offset:         0
        .size:           8
        .value_kind:     global_buffer
      - .actual_access:  read_only
        .address_space:  global
        .offset:         8
        .size:           8
        .value_kind:     global_buffer
      - .actual_access:  read_only
        .address_space:  global
        .offset:         16
        .size:           8
        .value_kind:     global_buffer
      - .actual_access:  write_only
        .address_space:  global
        .offset:         24
        .size:           8
        .value_kind:     global_buffer
    .group_segment_fixed_size: 0
    .kernarg_segment_align: 8
    .kernarg_segment_size: 32
    .language:       OpenCL C
    .language_version:
      - 2
      - 0
    .max_flat_workgroup_size: 256
    .name:           _Z9k_combinePKDF16_PK15HIP_vector_typeIiLj2EEPKS1_IfLj2EEPf
    .private_segment_fixed_size: 0
    .sgpr_count:     30
    .sgpr_spill_count: 0
    .symbol:         _Z9k_combinePKDF16_PK15HIP_vector_typeIiLj2EEPKS1_IfLj2EEPf.kd
    .uniform_work_group_size: 1
    .uses_dynamic_stack: false
    .vgpr_count:     64
    .vgpr_spill_count: 0
    .wavefront_size: 64
  - .agpr_count:     0
    .args:
      - .address_space:  global
        .offset:         0
        .size:           8
        .value_kind:     global_buffer
      - .address_space:  global
        .offset:         8
        .size:           8
        .value_kind:     global_buffer
      - .actual_access:  write_only
        .address_space:  global
        .offset:         16
        .size:           8
        .value_kind:     global_buffer
      - .actual_access:  read_only
        .address_space:  global
        .offset:         24
        .size:           8
        .value_kind:     global_buffer
      - .address_space:  global
        .offset:         32
        .size:           8
        .value_kind:     global_buffer
      - .address_space:  global
        .offset:         40
        .size:           8
        .value_kind:     global_buffer
      - .actual_access:  write_only
        .address_space:  global
        .offset:         48
        .size:           8
        .value_kind:     global_buffer
      - .address_space:  global
        .offset:         56
        .size:           8
        .value_kind:     global_buffer
    .group_segment_fixed_size: 0
    .kernarg_segment_align: 8
    .kernarg_segment_size: 64
    .language:       OpenCL C
    .language_version:
      - 2
      - 0
    .max_flat_workgroup_size: 512
    .name:           _Z7k_gemm1ILi0EEvPKDF16_S1_PDF16_PK15HIP_vector_typeIiLj2EEPKfS8_S2_PKt
    .private_segment_fixed_size: 0
    .sgpr_count:     102
    .sgpr_spill_count: 0
    .symbol:         _Z7k_gemm1ILi0EEvPKDF16_S1_PDF16_PK15HIP_vector_typeIiLj2EEPKfS8_S2_PKt.kd
    .uniform_work_group_size: 1
    .uses_dynamic_stack: false
    .vgpr_count:     256
    .vgpr_spill_count: 0
    .wavefront_size: 64
  - .agpr_count:     0
    .args:
      - .address_space:  global
        .offset:         0
        .size:           8
        .value_kind:     global_buffer
      - .address_space:  global
        .offset:         8
        .size:           8
        .value_kind:     global_buffer
      - .actual_access:  write_only
        .address_space:  global
        .offset:         16
        .size:           8
        .value_kind:     global_buffer
      - .actual_access:  read_only
        .address_space:  global
        .offset:         24
        .size:           8
        .value_kind:     global_buffer
      - .address_space:  global
        .offset:         32
        .size:           8
        .value_kind:     global_buffer
      - .actual_access:  read_only
        .address_space:  global
        .offset:         40
        .size:           8
        .value_kind:     global_buffer
      - .actual_access:  write_only
        .address_space:  global
        .offset:         48
        .size:           8
        .value_kind:     global_buffer
      - .address_space:  global
        .offset:         56
        .size:           8
        .value_kind:     global_buffer
    .group_segment_fixed_size: 0
    .kernarg_segment_align: 8
    .kernarg_segment_size: 64
    .language:       OpenCL C
    .language_version:
      - 2
      - 0
    .max_flat_workgroup_size: 512
    .name:           _Z7k_gemm1ILi1EEvPKDF16_S1_PDF16_PK15HIP_vector_typeIiLj2EEPKfS8_S2_PKt
    .private_segment_fixed_size: 0
    .sgpr_count:     96
    .sgpr_spill_count: 0
    .symbol:         _Z7k_gemm1ILi1EEvPKDF16_S1_PDF16_PK15HIP_vector_typeIiLj2EEPKfS8_S2_PKt.kd
    .uniform_work_group_size: 1
    .uses_dynamic_stack: false
    .vgpr_count:     254
    .vgpr_spill_count: 0
    .wavefront_size: 64
